# barrier: leader issues wbl2 then L1 invalidate back to back before one wait (invalidate hidden under the write-back)
# speedup vs baseline: 1.0028x; 1.0028x over previous
; __device__ __forceinline__ unsigned xb_ld(unsigned* p)              { return __hip_atomic_load(p, __ATOMIC_RELAXED, __HIP_MEMORY_SCOPE_AGENT); }
; __device__ __forceinline__ unsigned xb_add(unsigned* p, unsigned v) { return __hip_atomic_fetch_add(p, v, __ATOMIC_RELAXED, __HIP_MEMORY_SCOPE_AGENT); }
; #define XB_SPIN(cond, bar) do { unsigned _sp = 0; while (cond) { __builtin_amdgcn_s_sleep(1); \
;     if ((++_sp & 255u) == 0u) { if (xb_ld(&(bar)[XB_TMO])) break; if (_sp > XB_SPIN_CAP) { atomicAdd(&(bar)[XB_TMO], 1u); break; } } } } while (0)
; __device__ __forceinline__ void xcd_barrier(const XcdBarrier& b) {
;     ...
;         unsigned nloc = b.st[0], nx = b.st[1];
;         if (nloc == 0u) { xcd_barrier_complete(bar, b.x, nloc, nx); b.st[0] = nloc; b.st[1] = nx; }
;         const unsigned old = xb_add(&bar[XB_XSUB(b.x)], one_);
;         const unsigned gen = old / nloc;
;         if (old + 1u == (gen + 1u) * nloc) {
;             __builtin_amdgcn_fence(__ATOMIC_RELEASE, "agent");
;             asm volatile("s_waitcnt vmcnt(0)" ::: "memory");
;             const unsigned og = xb_add(&bar[XB_TOP], one_);
;             const unsigned tg = og / nx;
;             if (og + 1u == (tg + 1u) * nx) xb_add(&bar[XB_TOPGEN], one_);
;             else XB_SPIN(xb_ld(&bar[XB_TOPGEN]) == tg, bar);
;             __builtin_amdgcn_fence(__ATOMIC_ACQUIRE, "agent");
;             xb_add(&bar[XB_XGEN(b.x)], one_);
;             asm volatile("s_waitcnt vmcnt(0)" ::: "memory");
;         } else {
;             XB_SPIN(xb_ld(&bar[XB_XGEN(b.x)]) == gen, bar);
;             __builtin_amdgcn_fence(__ATOMIC_ACQUIRE, "agent");
;             asm volatile("s_waitcnt vmcnt(0)" ::: "memory");
;         }
.LBB0_142:
	s_lshl_b32 s2, s33, 8
	s_add_u32 s23, s34, s2
	s_addc_u32 s22, s35, 0
	v_mov_b32_e32 v1, s23
	v_add_co_u32_e32 v4, vcc, 0x1000, v1
	v_mov_b32_e32 v1, s22
	s_nop 0
	v_addc_co_u32_e32 v5, vcc, 0, v1, vcc
	flat_atomic_add v1, v[4:5], v10 offset:1024 sc0
	v_cvt_f32_u32_e32 v3, v2
	v_sub_u32_e32 v4, 0, v2
	v_rcp_iflag_f32_e32 v3, v3
	s_nop 0
	v_mul_f32_e32 v3, 0x4f7ffffe, v3
	v_cvt_u32_f32_e32 v3, v3
	v_mul_lo_u32 v4, v4, v3
	v_mul_hi_u32 v4, v3, v4
	v_add_u32_e32 v3, v3, v4
	s_waitcnt vmcnt(0) lgkmcnt(0)
	v_mul_hi_u32 v3, v1, v3
	v_mul_lo_u32 v5, v3, v2
	v_add_u32_e32 v4, 1, v1
	v_sub_u32_e32 v1, v1, v5
	v_add_u32_e32 v6, 1, v3
	v_cmp_ge_u32_e32 vcc, v1, v2
	v_sub_u32_e32 v5, v1, v2
	s_nop 0
	v_cndmask_b32_e32 v3, v3, v6, vcc
	v_cndmask_b32_e32 v1, v1, v5, vcc
	v_add_u32_e32 v5, 1, v3
	v_cmp_ge_u32_e32 vcc, v1, v2
	s_nop 1
	v_cndmask_b32_e32 v1, v3, v5, vcc
	v_mad_u64_u32 v[2:3], s[2:3], v2, v1, v[2:3]
	v_cmp_ne_u32_e32 vcc, v4, v2
	v_mov_b32_e32 v20, 0
	s_cbranch_vccnz .Lxbar0_nl
	buffer_wbl2 sc1
	buffer_inv sc1
	s_waitcnt vmcnt(0)
	s_sub_u32 s2, s23, s34
	s_lshr_b32 s2, s2, 6
	s_add_u32 s6, s34, 0x2400
	s_addc_u32 s7, s35, 0
	s_add_u32 s6, s6, s2
	s_addc_u32 s7, s7, 0
	global_atomic_add v20, v10, s[6:7]
	s_branch .Lxbar0_poll

; __device__ __forceinline__ unsigned xb_ld(unsigned* p)              { return __hip_atomic_load(p, __ATOMIC_RELAXED, __HIP_MEMORY_SCOPE_AGENT); }
; __device__ __forceinline__ unsigned xb_add(unsigned* p, unsigned v) { return __hip_atomic_fetch_add(p, v, __ATOMIC_RELAXED, __HIP_MEMORY_SCOPE_AGENT); }
; #define XB_SPIN(cond, bar) do { unsigned _sp = 0; while (cond) { __builtin_amdgcn_s_sleep(1); \
;     if ((++_sp & 255u) == 0u) { if (xb_ld(&(bar)[XB_TMO])) break; if (_sp > XB_SPIN_CAP) { atomicAdd(&(bar)[XB_TMO], 1u); break; } } } } while (0)
; __device__ __forceinline__ void xcd_barrier(const XcdBarrier& b) {
;     ...
;         unsigned nloc = b.st[0], nx = b.st[1];
;         if (nloc == 0u) { xcd_barrier_complete(bar, b.x, nloc, nx); b.st[0] = nloc; b.st[1] = nx; }
;         const unsigned old = xb_add(&bar[XB_XSUB(b.x)], one_);
;         const unsigned gen = old / nloc;
;         if (old + 1u == (gen + 1u) * nloc) {
;             __builtin_amdgcn_fence(__ATOMIC_RELEASE, "agent");
;             asm volatile("s_waitcnt vmcnt(0)" ::: "memory");
;             const unsigned og = xb_add(&bar[XB_TOP], one_);
;             const unsigned tg = og / nx;
;             if (og + 1u == (tg + 1u) * nx) xb_add(&bar[XB_TOPGEN], one_);
;             else XB_SPIN(xb_ld(&bar[XB_TOPGEN]) == tg, bar);
;             __builtin_amdgcn_fence(__ATOMIC_ACQUIRE, "agent");
;             xb_add(&bar[XB_XGEN(b.x)], one_);
;             asm volatile("s_waitcnt vmcnt(0)" ::: "memory");
;         } else {
;             XB_SPIN(xb_ld(&bar[XB_XGEN(b.x)]) == gen, bar);
;             __builtin_amdgcn_fence(__ATOMIC_ACQUIRE, "agent");
;             asm volatile("s_waitcnt vmcnt(0)" ::: "memory");
;         }
.LBB0_430:
	v_readlane_b32 s4, v253, 57
	s_lshl_b32 s4, s4, 2
	s_add_u32 s25, s2, s4
	s_addc_u32 s24, s3, 0
	v_mov_b32_e32 v3, s25
	v_add_co_u32_e32 v6, vcc, 0x1000, v3
	v_mov_b32_e32 v3, s24
	s_nop 0
	v_addc_co_u32_e32 v7, vcc, 0, v3, vcc
	flat_atomic_add v5, v[6:7], v1 offset:1024 sc0
	v_cvt_f32_u32_e32 v3, v4
	v_sub_u32_e32 v6, 0, v4
	v_rcp_iflag_f32_e32 v3, v3
	s_nop 0
	v_mul_f32_e32 v3, 0x4f7ffffe, v3
	v_cvt_u32_f32_e32 v3, v3
	v_mul_lo_u32 v6, v6, v3
	v_mul_hi_u32 v6, v3, v6
	v_add_u32_e32 v3, v3, v6
	s_waitcnt vmcnt(0) lgkmcnt(0)
	v_mul_hi_u32 v3, v5, v3
	v_mul_lo_u32 v6, v3, v4
	v_sub_u32_e32 v6, v5, v6
	v_cmp_ge_u32_e32 vcc, v6, v4
	v_add_u32_e32 v7, 1, v3
	s_nop 0
	v_cndmask_b32_e32 v3, v3, v7, vcc
	v_sub_u32_e32 v7, v6, v4
	v_cndmask_b32_e32 v6, v6, v7, vcc
	v_cmp_ge_u32_e32 vcc, v6, v4
	v_add_u32_e32 v6, 1, v3
	s_nop 0
	v_cndmask_b32_e32 v3, v3, v6, vcc
	v_add_u32_e32 v6, 1, v5
	v_mad_u64_u32 v[4:5], s[4:5], v4, v3, v[4:5]
	v_cmp_ne_u32_e32 vcc, v6, v4
	v_mov_b32_e32 v20, 0
	s_cbranch_vccnz .Lxbar1_nl
	buffer_wbl2 sc1
	buffer_inv sc1
	s_waitcnt vmcnt(0)
	s_sub_u32 s4, s25, s2
	s_lshr_b32 s4, s4, 6
	s_add_u32 s8, s2, 0x2400
	s_addc_u32 s9, s3, 0
	s_add_u32 s8, s8, s4
	s_addc_u32 s9, s9, 0
	global_atomic_add v20, v1, s[8:9]
	s_branch .Lxbar1_poll

; __device__ __forceinline__ unsigned xb_ld(unsigned* p)              { return __hip_atomic_load(p, __ATOMIC_RELAXED, __HIP_MEMORY_SCOPE_AGENT); }
; __device__ __forceinline__ unsigned xb_add(unsigned* p, unsigned v) { return __hip_atomic_fetch_add(p, v, __ATOMIC_RELAXED, __HIP_MEMORY_SCOPE_AGENT); }
; #define XB_SPIN(cond, bar) do { unsigned _sp = 0; while (cond) { __builtin_amdgcn_s_sleep(1); \
;     if ((++_sp & 255u) == 0u) { if (xb_ld(&(bar)[XB_TMO])) break; if (_sp > XB_SPIN_CAP) { atomicAdd(&(bar)[XB_TMO], 1u); break; } } } } while (0)
; __device__ __forceinline__ void xcd_barrier(const XcdBarrier& b) {
;     ...
;         unsigned nloc = b.st[0], nx = b.st[1];
;         if (nloc == 0u) { xcd_barrier_complete(bar, b.x, nloc, nx); b.st[0] = nloc; b.st[1] = nx; }
;         const unsigned old = xb_add(&bar[XB_XSUB(b.x)], one_);
;         const unsigned gen = old / nloc;
;         if (old + 1u == (gen + 1u) * nloc) {
;             __builtin_amdgcn_fence(__ATOMIC_RELEASE, "agent");
;             asm volatile("s_waitcnt vmcnt(0)" ::: "memory");
;             const unsigned og = xb_add(&bar[XB_TOP], one_);
;             const unsigned tg = og / nx;
;             if (og + 1u == (tg + 1u) * nx) xb_add(&bar[XB_TOPGEN], one_);
;             else XB_SPIN(xb_ld(&bar[XB_TOPGEN]) == tg, bar);
;             __builtin_amdgcn_fence(__ATOMIC_ACQUIRE, "agent");
;             xb_add(&bar[XB_XGEN(b.x)], one_);
;             asm volatile("s_waitcnt vmcnt(0)" ::: "memory");
;         } else {
;             XB_SPIN(xb_ld(&bar[XB_XGEN(b.x)]) == gen, bar);
;             __builtin_amdgcn_fence(__ATOMIC_ACQUIRE, "agent");
;             asm volatile("s_waitcnt vmcnt(0)" ::: "memory");
;         }
.LBB0_681:
	v_readlane_b32 s6, v253, 57
	s_lshl_b32 s6, s6, 2
	s_add_u32 s27, s4, s6
	s_addc_u32 s26, s5, 0
	v_mov_b32_e32 v3, s27
	v_add_co_u32_e32 v6, vcc, 0x1000, v3
	v_mov_b32_e32 v3, s26
	s_nop 0
	v_addc_co_u32_e32 v7, vcc, 0, v3, vcc
	flat_atomic_add v5, v[6:7], v1 offset:1024 sc0
	v_cvt_f32_u32_e32 v3, v4
	v_sub_u32_e32 v6, 0, v4
	v_rcp_iflag_f32_e32 v3, v3
	s_nop 0
	v_mul_f32_e32 v3, 0x4f7ffffe, v3
	v_cvt_u32_f32_e32 v3, v3
	v_mul_lo_u32 v6, v6, v3
	v_mul_hi_u32 v6, v3, v6
	v_add_u32_e32 v3, v3, v6
	s_waitcnt vmcnt(0) lgkmcnt(0)
	v_mul_hi_u32 v3, v5, v3
	v_mul_lo_u32 v6, v3, v4
	v_sub_u32_e32 v6, v5, v6
	v_cmp_ge_u32_e32 vcc, v6, v4
	v_add_u32_e32 v7, 1, v3
	s_nop 0
	v_cndmask_b32_e32 v3, v3, v7, vcc
	v_sub_u32_e32 v7, v6, v4
	v_cndmask_b32_e32 v6, v6, v7, vcc
	v_cmp_ge_u32_e32 vcc, v6, v4
	v_add_u32_e32 v6, 1, v3
	s_nop 0
	v_cndmask_b32_e32 v3, v3, v6, vcc
	v_add_u32_e32 v6, 1, v5
	v_mad_u64_u32 v[4:5], s[6:7], v4, v3, v[4:5]
	v_cmp_ne_u32_e32 vcc, v6, v4
	v_mov_b32_e32 v20, 0
	s_cbranch_vccnz .Lxbar2_nl
	buffer_wbl2 sc1
	buffer_inv sc1
	s_waitcnt vmcnt(0)
	s_sub_u32 s6, s27, s4
	s_lshr_b32 s6, s6, 6
	s_add_u32 s10, s4, 0x2400
	s_addc_u32 s11, s5, 0
	s_add_u32 s10, s10, s6
	s_addc_u32 s11, s11, 0
	global_atomic_add v20, v1, s[10:11]
	s_branch .Lxbar2_poll

; __device__ __forceinline__ unsigned xb_ld(unsigned* p)              { return __hip_atomic_load(p, __ATOMIC_RELAXED, __HIP_MEMORY_SCOPE_AGENT); }
; __device__ __forceinline__ unsigned xb_add(unsigned* p, unsigned v) { return __hip_atomic_fetch_add(p, v, __ATOMIC_RELAXED, __HIP_MEMORY_SCOPE_AGENT); }
; #define XB_SPIN(cond, bar) do { unsigned _sp = 0; while (cond) { __builtin_amdgcn_s_sleep(1); \
;     if ((++_sp & 255u) == 0u) { if (xb_ld(&(bar)[XB_TMO])) break; if (_sp > XB_SPIN_CAP) { atomicAdd(&(bar)[XB_TMO], 1u); break; } } } } while (0)
; __device__ __forceinline__ void xcd_barrier(const XcdBarrier& b) {
;     ...
;         unsigned nloc = b.st[0], nx = b.st[1];
;         if (nloc == 0u) { xcd_barrier_complete(bar, b.x, nloc, nx); b.st[0] = nloc; b.st[1] = nx; }
;         const unsigned old = xb_add(&bar[XB_XSUB(b.x)], one_);
;         const unsigned gen = old / nloc;
;         if (old + 1u == (gen + 1u) * nloc) {
;             __builtin_amdgcn_fence(__ATOMIC_RELEASE, "agent");
;             asm volatile("s_waitcnt vmcnt(0)" ::: "memory");
;             const unsigned og = xb_add(&bar[XB_TOP], one_);
;             const unsigned tg = og / nx;
;             if (og + 1u == (tg + 1u) * nx) xb_add(&bar[XB_TOPGEN], one_);
;             else XB_SPIN(xb_ld(&bar[XB_TOPGEN]) == tg, bar);
;             __builtin_amdgcn_fence(__ATOMIC_ACQUIRE, "agent");
;             xb_add(&bar[XB_XGEN(b.x)], one_);
.LBB0_928:
	v_readlane_b32 s6, v253, 57
	s_lshl_b32 s6, s6, 2
	s_add_u32 s29, s4, s6
	s_addc_u32 s28, s5, 0
	v_mov_b32_e32 v3, s29
	v_add_co_u32_e32 v6, vcc, 0x1000, v3
	v_mov_b32_e32 v3, s28
	s_nop 0
	v_addc_co_u32_e32 v7, vcc, 0, v3, vcc
	flat_atomic_add v5, v[6:7], v1 offset:1024 sc0
	v_cvt_f32_u32_e32 v3, v4
	v_sub_u32_e32 v6, 0, v4
	v_rcp_iflag_f32_e32 v3, v3
	s_nop 0
	v_mul_f32_e32 v3, 0x4f7ffffe, v3
	v_cvt_u32_f32_e32 v3, v3
	v_mul_lo_u32 v6, v6, v3
	v_mul_hi_u32 v6, v3, v6
	v_add_u32_e32 v3, v3, v6
	s_waitcnt vmcnt(0) lgkmcnt(0)
	v_mul_hi_u32 v3, v5, v3
	v_mul_lo_u32 v6, v3, v4
	v_sub_u32_e32 v6, v5, v6
	v_cmp_ge_u32_e32 vcc, v6, v4
	v_add_u32_e32 v7, 1, v3
	s_nop 0
	v_cndmask_b32_e32 v3, v3, v7, vcc
	v_sub_u32_e32 v7, v6, v4
	v_cndmask_b32_e32 v6, v6, v7, vcc
	v_cmp_ge_u32_e32 vcc, v6, v4
	v_add_u32_e32 v6, 1, v3
	s_nop 0
	v_cndmask_b32_e32 v3, v3, v6, vcc
	v_add_u32_e32 v6, 1, v5
	v_mad_u64_u32 v[4:5], s[6:7], v4, v3, v[4:5]
	v_cmp_ne_u32_e32 vcc, v6, v4
	v_mov_b32_e32 v20, 0
	s_cbranch_vccnz .Lxbar4_nl
	buffer_wbl2 sc1
	buffer_inv sc1
	s_waitcnt vmcnt(0)
	s_sub_u32 s6, s29, s4
	s_lshr_b32 s6, s6, 6
	s_add_u32 s10, s4, 0x2400
	s_addc_u32 s11, s5, 0
	s_add_u32 s10, s10, s6
	s_addc_u32 s11, s11, 0
	global_atomic_add v20, v1, s[10:11]
	s_branch .Lxbar4_poll

; __device__ __forceinline__ unsigned xb_ld(unsigned* p)              { return __hip_atomic_load(p, __ATOMIC_RELAXED, __HIP_MEMORY_SCOPE_AGENT); }
; __device__ __forceinline__ unsigned xb_add(unsigned* p, unsigned v) { return __hip_atomic_fetch_add(p, v, __ATOMIC_RELAXED, __HIP_MEMORY_SCOPE_AGENT); }
; #define XB_SPIN(cond, bar) do { unsigned _sp = 0; while (cond) { __builtin_amdgcn_s_sleep(1); \
;     if ((++_sp & 255u) == 0u) { if (xb_ld(&(bar)[XB_TMO])) break; if (_sp > XB_SPIN_CAP) { atomicAdd(&(bar)[XB_TMO], 1u); break; } } } } while (0)
; __device__ __forceinline__ void xcd_barrier(const XcdBarrier& b) {
;     ...
;         unsigned nloc = b.st[0], nx = b.st[1];
;         if (nloc == 0u) { xcd_barrier_complete(bar, b.x, nloc, nx); b.st[0] = nloc; b.st[1] = nx; }
;         const unsigned old = xb_add(&bar[XB_XSUB(b.x)], one_);
;         const unsigned gen = old / nloc;
;         if (old + 1u == (gen + 1u) * nloc) {
;             __builtin_amdgcn_fence(__ATOMIC_RELEASE, "agent");
;             asm volatile("s_waitcnt vmcnt(0)" ::: "memory");
;             const unsigned og = xb_add(&bar[XB_TOP], one_);
;             const unsigned tg = og / nx;
;             if (og + 1u == (tg + 1u) * nx) xb_add(&bar[XB_TOPGEN], one_);
;             else XB_SPIN(xb_ld(&bar[XB_TOPGEN]) == tg, bar);
;             __builtin_amdgcn_fence(__ATOMIC_ACQUIRE, "agent");
;             xb_add(&bar[XB_XGEN(b.x)], one_);
.LBB0_1016:
	v_readlane_b32 s4, v253, 57
	s_lshl_b32 s4, s4, 2
	s_add_u32 s27, s2, s4
	s_addc_u32 s26, s3, 0
	v_mov_b32_e32 v3, s27
	v_add_co_u32_e32 v6, vcc, 0x1000, v3
	v_mov_b32_e32 v3, s26
	s_nop 0
	v_addc_co_u32_e32 v7, vcc, 0, v3, vcc
	flat_atomic_add v5, v[6:7], v1 offset:1024 sc0
	v_cvt_f32_u32_e32 v3, v4
	v_sub_u32_e32 v6, 0, v4
	v_rcp_iflag_f32_e32 v3, v3
	s_nop 0
	v_mul_f32_e32 v3, 0x4f7ffffe, v3
	v_cvt_u32_f32_e32 v3, v3
	v_mul_lo_u32 v6, v6, v3
	v_mul_hi_u32 v6, v3, v6
	v_add_u32_e32 v3, v3, v6
	s_waitcnt vmcnt(0) lgkmcnt(0)
	v_mul_hi_u32 v3, v5, v3
	v_mul_lo_u32 v6, v3, v4
	v_sub_u32_e32 v6, v5, v6
	v_cmp_ge_u32_e32 vcc, v6, v4
	v_add_u32_e32 v7, 1, v3
	s_nop 0
	v_cndmask_b32_e32 v3, v3, v7, vcc
	v_sub_u32_e32 v7, v6, v4
	v_cndmask_b32_e32 v6, v6, v7, vcc
	v_cmp_ge_u32_e32 vcc, v6, v4
	v_add_u32_e32 v6, 1, v3
	s_nop 0
	v_cndmask_b32_e32 v3, v3, v6, vcc
	v_add_u32_e32 v6, 1, v5
	v_mad_u64_u32 v[4:5], s[4:5], v4, v3, v[4:5]
	v_cmp_ne_u32_e32 vcc, v6, v4
	v_mov_b32_e32 v20, 0
	s_cbranch_vccnz .Lxbar5_nl
	buffer_wbl2 sc1
	buffer_inv sc1
	s_waitcnt vmcnt(0)
	s_sub_u32 s4, s27, s2
	s_lshr_b32 s4, s4, 6
	s_add_u32 s8, s2, 0x2400
	s_addc_u32 s9, s3, 0
	s_add_u32 s8, s8, s4
	s_addc_u32 s9, s9, 0
	global_atomic_add v20, v1, s[8:9]
	s_branch .Lxbar5_poll
